# baseline (speedup 1.0000x reference)
_Z13prep_w_kernelPKfS0_S0_PDv8_DF16_:
	s_load_dwordx8 s[4:11], s[0:1], 0x0
	s_lshl_b32 s2, s2, 6
	v_add_u32_e32 v0, s2, v0
	s_movk_i32 s2, 0x6000
	v_cmp_gt_i32_e32 vcc, s2, v0
	s_and_saveexec_b64 s[2:3], vcc
	s_cbranch_execz .LBB0_2
	v_ashrrev_i32_e32 v1, 6, v0
	s_mov_b32 s0, 0x55555556
	v_mul_hi_i32 v2, v1, s0
	v_lshrrev_b32_e32 v3, 31, v2
	v_add_u32_e32 v4, v2, v3
	v_lshl_add_u32 v2, v4, 1, v4
	s_mov_b32 s0, 0x2aaaaaab
	v_sub_u32_e32 v2, v1, v2
	v_mul_hi_i32 v1, v1, s0
	v_lshrrev_b32_e32 v3, 31, v1
	v_lshrrev_b32_e32 v1, 4, v1
	v_add_u32_e32 v1, v1, v3
	s_waitcnt lgkmcnt(0)
	v_mov_b32_e32 v3, s8
	v_mov_b32_e32 v5, s6
	v_cmp_eq_u32_e32 vcc, 1, v2
	v_mov_b32_e32 v6, s7
	v_lshlrev_b32_e32 v4, 5, v4
	v_cndmask_b32_e32 v5, v3, v5, vcc
	v_mov_b32_e32 v3, s9
	v_cndmask_b32_e32 v3, v3, v6, vcc
	v_cmp_eq_u32_e32 vcc, 0, v2
	v_mov_b32_e32 v2, s5
	v_and_b32_e32 v4, 0x3e0, v4
	v_cndmask_b32_e32 v3, v3, v2, vcc
	v_mov_b32_e32 v2, s4
	v_cndmask_b32_e32 v2, v5, v2, vcc
	v_lshrrev_b32_e32 v5, 1, v0
	v_and_or_b32 v5, v5, 24, v4
	v_and_b32_e32 v4, 15, v0
	v_lshl_or_b32 v4, v1, 4, v4
	v_lshlrev_b32_e32 v8, 6, v5
	v_add_u32_e32 v10, v4, v8
	v_ashrrev_i32_e32 v11, 31, v10
	v_ashrrev_i32_e32 v5, 31, v4
	v_mov_b32_e32 v9, 0
	v_mov_b32_e32 v6, 0x42800000
	v_mov_b32_e32 v7, 0x4138aa3b
	v_lshl_add_u64 v[10:11], v[10:11], 2, v[2:3]
	v_lshl_add_u64 v[4:5], v[4:5], 0, v[8:9]
	v_cndmask_b32_e32 v6, v6, v7, vcc
	v_lshl_add_u64 v[2:3], v[4:5], 2, v[2:3]
	global_load_dword v7, v[10:11], off
	global_load_dword v4, v[2:3], off offset:256
	global_load_dword v5, v[2:3], off offset:512
	global_load_dword v8, v[2:3], off offset:768
	global_load_dword v9, v[2:3], off offset:1024
	global_load_dword v12, v[2:3], off offset:1280
	global_load_dword v13, v[2:3], off offset:1536
	global_load_dword v14, v[2:3], off offset:1792
	v_ashrrev_i32_e32 v1, 31, v0
	v_lshl_add_u64 v[0:1], v[0:1], 4, s[10:11]
	s_waitcnt vmcnt(7)
	v_fma_mixlo_f16 v7, v6, v7, 0
	s_waitcnt vmcnt(5)
	v_pk_mul_f32 v[2:3], v[6:7], v[4:5] op_sel_hi:[0,1]
	v_cvt_pk_f16_f32 v3, v2, v3
	s_waitcnt vmcnt(3)
	v_pk_mul_f32 v[4:5], v[6:7], v[8:9] op_sel_hi:[0,1]
	v_cvt_pk_f16_f32 v4, v4, v5
	s_waitcnt vmcnt(1)
	v_pk_mul_f32 v[8:9], v[6:7], v[12:13] op_sel_hi:[0,1]
	v_cvt_pk_f16_f32 v5, v8, v9
	v_pack_b32_f16 v2, v7, v3
	v_alignbit_b32 v3, v4, v3, 16
	v_alignbit_b32 v4, v5, v4, 16
	v_lshrrev_b32_e32 v5, 16, v5
	s_waitcnt vmcnt(0)
	v_fma_mixhi_f16 v5, v6, v14, 0
	global_store_dwordx4 v[0:1], v[2:5], off

.LBB2_12:
	s_xor_b64 s[38:39], s[38:39], -1
	v_max3_f32 v69, v46, v47, v48
	s_and_b64 vcc, exec, s[38:39]
	v_max3_f32 v69, v69, v49, v42
	s_nop 0
	v_max3_f32 v69, v69, v43, v44
	v_max3_f32 v69, v69, v45, v38
	v_max3_f32 v69, v69, v39, v40
	v_max3_f32 v69, v69, v41, v34
	v_max3_f32 v69, v69, v35, v36
	v_max_f32_e32 v69, v69, v37
	v_mov_b32_e32 v71, v69
	s_nop 1
	v_permlane16_swap_b32_e32 v69, v71
	v_max_f32_e32 v69, v69, v71
	v_mov_b32_e32 v71, v69
	s_nop 1
	v_permlane32_swap_b32_e32 v69, v71
	v_max_f32_e32 v69, v69, v71
	s_cbranch_vccz .LBB2_19
	v_cmp_lt_f32_e32 vcc, s58, v69
	s_mov_b64 s[48:49], 0
	s_mov_b64 s[38:39], 0
	s_cbranch_vccz .LBB2_15
	v_max_f32_e32 v71, v69, v69
	v_max_f32_e32 v80, 0, v71
	s_mov_b64 s[38:39], -1

_Z14combine_kernelPKDF16_PKfPf:
	s_load_dwordx4 s[4:7], s[0:1], 0x0
	s_load_dwordx2 s[10:11], s[0:1], 0x10
	s_lshl_b32 s3, s2, 5
	s_and_b32 s3, s3, 0x60
	s_lshr_b32 s8, s2, 5
	s_add_i32 s8, s8, s3
	s_lshl_b32 s9, s8, 5
	s_getpc_b64 s[12:13]
	s_add_u32 s12, s12, g_tab@rel32@lo+4
	s_addc_u32 s13, s13, g_tab@rel32@hi+12
	s_add_u32 s12, s12, s9
	s_addc_u32 s13, s13, 0
	s_load_dwordx8 s[16:23], s[12:13], 0x1a60
	s_lshl_b32 s2, s2, 2
	s_and_b32 s2, s2, 0x70
	v_lshrrev_b32_e32 v1, 4, v0
	v_or_b32_e32 v38, s2, v1
	v_lshlrev_b32_e32 v2, 2, v0
	v_and_b32_e32 v39, 60, v2
	v_lshlrev_b32_e32 v32, 3, v38
	v_lshlrev_b32_e32 v33, 7, v38
	v_lshl_add_u32 v33, v39, 1, v33
	v_lshlrev_b32_e32 v45, 8, v38
	v_lshl_add_u32 v45, v39, 2, v45
	s_add_i32 s0, s8, 3
	s_lshl_b32 s0, s0, 15
	s_mov_b32 s14, 0x7f800000
	s_mov_b32 s15, 0xf149f2ca
	s_waitcnt lgkmcnt(0)
	s_cmp_lt_i32 s17, 0
	s_cbranch_scc1 .Lcomb_end
	s_add_u32 s10, s10, s0
	s_addc_u32 s11, s11, 0
	s_lshl_b32 s24, s16, 10
	s_lshl_b32 s26, s16, 14
	s_add_u32 s24, s6, s24
	s_addc_u32 s25, s7, 0
	s_add_u32 s26, s4, s26
	s_addc_u32 s27, s5, 0
	global_load_dwordx2 v[0:1], v32, s[24:25] nt
	global_load_dwordx2 v[16:17], v33, s[26:27] nt
	s_lshl_b32 s28, s17, 10
	s_lshl_b32 s30, s17, 14
	s_add_u32 s28, s6, s28
	s_addc_u32 s29, s7, 0
	s_add_u32 s30, s4, s30
	s_addc_u32 s31, s5, 0
	global_load_dwordx2 v[2:3], v32, s[28:29] nt
	global_load_dwordx2 v[18:19], v33, s[30:31] nt
	s_cmp_lt_i32 s18, 0
	s_cselect_b32 s58, s15, s14
	s_cselect_b32 s1, s16, s18
	s_lshl_b32 s32, s1, 10
	s_lshl_b32 s34, s1, 14
	s_add_u32 s32, s6, s32
	s_addc_u32 s33, s7, 0
	s_add_u32 s34, s4, s34
	s_addc_u32 s35, s5, 0
	global_load_dwordx2 v[4:5], v32, s[32:33] nt
	global_load_dwordx2 v[20:21], v33, s[34:35] nt
	s_cmp_lt_i32 s19, 0
	s_cselect_b32 s59, s15, s14
	s_cselect_b32 s1, s16, s19
	s_lshl_b32 s36, s1, 10
	s_lshl_b32 s38, s1, 14
	s_add_u32 s36, s6, s36
	s_addc_u32 s37, s7, 0
	s_add_u32 s38, s4, s38
	s_addc_u32 s39, s5, 0
	global_load_dwordx2 v[6:7], v32, s[36:37] nt
	global_load_dwordx2 v[22:23], v33, s[38:39] nt
	s_cmp_lt_i32 s20, 0
	s_cselect_b32 s60, s15, s14
	s_cselect_b32 s1, s16, s20
	s_lshl_b32 s40, s1, 10
	s_lshl_b32 s42, s1, 14
	s_add_u32 s40, s6, s40
	s_addc_u32 s41, s7, 0
	s_add_u32 s42, s4, s42
	s_addc_u32 s43, s5, 0
	global_load_dwordx2 v[8:9], v32, s[40:41] nt
	global_load_dwordx2 v[24:25], v33, s[42:43] nt
	s_cmp_lt_i32 s21, 0
	s_cselect_b32 s61, s15, s14
	s_cselect_b32 s1, s16, s21
	s_lshl_b32 s44, s1, 10
	s_lshl_b32 s46, s1, 14
	s_add_u32 s44, s6, s44
	s_addc_u32 s45, s7, 0
	s_add_u32 s46, s4, s46
	s_addc_u32 s47, s5, 0
	global_load_dwordx2 v[10:11], v32, s[44:45] nt
	global_load_dwordx2 v[26:27], v33, s[46:47] nt
	s_cmp_lt_i32 s22, 0
	s_cselect_b32 s62, s15, s14
	s_cselect_b32 s1, s16, s22
	s_lshl_b32 s48, s1, 10
	s_lshl_b32 s50, s1, 14
	s_add_u32 s48, s6, s48
	s_addc_u32 s49, s7, 0
	s_add_u32 s50, s4, s50
	s_addc_u32 s51, s5, 0
	global_load_dwordx2 v[12:13], v32, s[48:49] nt
	global_load_dwordx2 v[28:29], v33, s[50:51] nt
	s_cmp_lt_i32 s23, 0
	s_cselect_b32 s63, s15, s14
	s_cselect_b32 s1, s16, s23
	s_lshl_b32 s52, s1, 10
	s_lshl_b32 s54, s1, 14
	s_add_u32 s52, s6, s52
	s_addc_u32 s53, s7, 0
	s_add_u32 s54, s4, s54
	s_addc_u32 s55, s5, 0
	global_load_dwordx2 v[14:15], v32, s[52:53] nt
	global_load_dwordx2 v[30:31], v33, s[54:55] nt
	s_waitcnt vmcnt(0)
	v_min_f32_e32 v4, s58, v4
	v_min_f32_e32 v6, s59, v6
	v_min_f32_e32 v8, s60, v8
	v_min_f32_e32 v10, s61, v10
	v_min_f32_e32 v12, s62, v12
	v_min_f32_e32 v14, s63, v14
	v_max3_f32 v34, v0, v2, v4
	v_max3_f32 v34, v34, v6, v8
	v_max3_f32 v34, v34, v10, v12
	v_max_f32_e32 v34, v34, v14
	v_sub_f32_e32 v0, v0, v34
	v_sub_f32_e32 v2, v2, v34
	v_sub_f32_e32 v4, v4, v34
	v_sub_f32_e32 v6, v6, v34
	v_sub_f32_e32 v8, v8, v34
	v_sub_f32_e32 v10, v10, v34
	v_sub_f32_e32 v12, v12, v34
	v_sub_f32_e32 v14, v14, v34
	v_exp_f32_e32 v0, v0
	v_exp_f32_e32 v2, v2
	v_exp_f32_e32 v4, v4
	v_exp_f32_e32 v6, v6
	v_exp_f32_e32 v8, v8
	v_exp_f32_e32 v10, v10
	v_exp_f32_e32 v12, v12
	v_exp_f32_e32 v14, v14
	s_nop 0
	v_mul_f32_e32 v0, v0, v1
	v_mul_f32_e32 v2, v2, v3
	v_mul_f32_e32 v4, v4, v5
	v_mul_f32_e32 v6, v6, v7
	v_mul_f32_e32 v8, v8, v9
	v_mul_f32_e32 v10, v10, v11
	v_mul_f32_e32 v12, v12, v13
	v_mul_f32_e32 v14, v14, v15
	v_cvt_f32_f16_e32 v40, v16
	v_cvt_f32_f16_sdwa v41, v16 dst_sel:DWORD dst_unused:UNUSED_PAD src0_sel:WORD_1
	v_cvt_f32_f16_e32 v42, v17
	v_cvt_f32_f16_sdwa v43, v17 dst_sel:DWORD dst_unused:UNUSED_PAD src0_sel:WORD_1
	v_mul_f32_e32 v34, v40, v0
	v_mul_f32_e32 v35, v41, v0
	v_mul_f32_e32 v36, v42, v0
	v_mul_f32_e32 v37, v43, v0
	v_mov_b32_e32 v44, v0
	v_cvt_f32_f16_e32 v40, v18
	v_cvt_f32_f16_sdwa v41, v18 dst_sel:DWORD dst_unused:UNUSED_PAD src0_sel:WORD_1
	v_cvt_f32_f16_e32 v42, v19
	v_cvt_f32_f16_sdwa v43, v19 dst_sel:DWORD dst_unused:UNUSED_PAD src0_sel:WORD_1
	v_fmac_f32_e32 v34, v40, v2
	v_fmac_f32_e32 v35, v41, v2
	v_fmac_f32_e32 v36, v42, v2
	v_fmac_f32_e32 v37, v43, v2
	v_add_f32_e32 v44, v44, v2
	v_cvt_f32_f16_e32 v40, v20
	v_cvt_f32_f16_sdwa v41, v20 dst_sel:DWORD dst_unused:UNUSED_PAD src0_sel:WORD_1
	v_cvt_f32_f16_e32 v42, v21
	v_cvt_f32_f16_sdwa v43, v21 dst_sel:DWORD dst_unused:UNUSED_PAD src0_sel:WORD_1
	v_fmac_f32_e32 v34, v40, v4
	v_fmac_f32_e32 v35, v41, v4
	v_fmac_f32_e32 v36, v42, v4
	v_fmac_f32_e32 v37, v43, v4
	v_add_f32_e32 v44, v44, v4
	v_cvt_f32_f16_e32 v40, v22
	v_cvt_f32_f16_sdwa v41, v22 dst_sel:DWORD dst_unused:UNUSED_PAD src0_sel:WORD_1
	v_cvt_f32_f16_e32 v42, v23
	v_cvt_f32_f16_sdwa v43, v23 dst_sel:DWORD dst_unused:UNUSED_PAD src0_sel:WORD_1
	v_fmac_f32_e32 v34, v40, v6
	v_fmac_f32_e32 v35, v41, v6
	v_fmac_f32_e32 v36, v42, v6
	v_fmac_f32_e32 v37, v43, v6
	v_add_f32_e32 v44, v44, v6
	v_cvt_f32_f16_e32 v40, v24
	v_cvt_f32_f16_sdwa v41, v24 dst_sel:DWORD dst_unused:UNUSED_PAD src0_sel:WORD_1
	v_cvt_f32_f16_e32 v42, v25
	v_cvt_f32_f16_sdwa v43, v25 dst_sel:DWORD dst_unused:UNUSED_PAD src0_sel:WORD_1
	v_fmac_f32_e32 v34, v40, v8
	v_fmac_f32_e32 v35, v41, v8
	v_fmac_f32_e32 v36, v42, v8
	v_fmac_f32_e32 v37, v43, v8
	v_add_f32_e32 v44, v44, v8
	v_cvt_f32_f16_e32 v40, v26
	v_cvt_f32_f16_sdwa v41, v26 dst_sel:DWORD dst_unused:UNUSED_PAD src0_sel:WORD_1
	v_cvt_f32_f16_e32 v42, v27
	v_cvt_f32_f16_sdwa v43, v27 dst_sel:DWORD dst_unused:UNUSED_PAD src0_sel:WORD_1
	v_fmac_f32_e32 v34, v40, v10
	v_fmac_f32_e32 v35, v41, v10
	v_fmac_f32_e32 v36, v42, v10
	v_fmac_f32_e32 v37, v43, v10
	v_add_f32_e32 v44, v44, v10
	v_cvt_f32_f16_e32 v40, v28
	v_cvt_f32_f16_sdwa v41, v28 dst_sel:DWORD dst_unused:UNUSED_PAD src0_sel:WORD_1
	v_cvt_f32_f16_e32 v42, v29
	v_cvt_f32_f16_sdwa v43, v29 dst_sel:DWORD dst_unused:UNUSED_PAD src0_sel:WORD_1
	v_fmac_f32_e32 v34, v40, v12
	v_fmac_f32_e32 v35, v41, v12
	v_fmac_f32_e32 v36, v42, v12
	v_fmac_f32_e32 v37, v43, v12
	v_add_f32_e32 v44, v44, v12
	v_cvt_f32_f16_e32 v40, v30
	v_cvt_f32_f16_sdwa v41, v30 dst_sel:DWORD dst_unused:UNUSED_PAD src0_sel:WORD_1
	v_cvt_f32_f16_e32 v42, v31
	v_cvt_f32_f16_sdwa v43, v31 dst_sel:DWORD dst_unused:UNUSED_PAD src0_sel:WORD_1
	v_fmac_f32_e32 v34, v40, v14
	v_fmac_f32_e32 v35, v41, v14
	v_fmac_f32_e32 v36, v42, v14
	v_fmac_f32_e32 v37, v43, v14
	v_add_f32_e32 v44, v44, v14
	v_div_scale_f32 v14, s[0:1], v44, v44, 1.0
	v_div_scale_f32 v2, vcc, 1.0, v44, 1.0
	v_rcp_f32_e32 v15, v14
	s_nop 0
	v_fma_f32 v3, -v14, v15, 1.0
	v_fmac_f32_e32 v15, v3, v15
	v_mul_f32_e32 v3, v2, v15
	v_fma_f32 v6, -v14, v3, v2
	v_fmac_f32_e32 v3, v6, v15
	v_fma_f32 v2, -v14, v3, v2
	v_div_fmas_f32 v2, v2, v15, v3
	v_div_fixup_f32 v6, v2, v44, 1.0
	v_mul_f32_e32 v34, v34, v6
	v_mul_f32_e32 v35, v35, v6
	v_mul_f32_e32 v36, v36, v6
	v_mul_f32_e32 v37, v37, v6
	global_store_dwordx4 v45, v[34:37], s[10:11] sc1

	.amdhsa_kernel _Z14combine_kernelPKDF16_PKfPf
		.amdhsa_group_segment_fixed_size 0
		.amdhsa_private_segment_fixed_size 0
		.amdhsa_kernarg_size 24
		.amdhsa_user_sgpr_count 2
		.amdhsa_user_sgpr_dispatch_ptr 0
		.amdhsa_user_sgpr_queue_ptr 0
		.amdhsa_user_sgpr_kernarg_segment_ptr 1
		.amdhsa_user_sgpr_dispatch_id 0
		.amdhsa_user_sgpr_kernarg_preload_length 0
		.amdhsa_user_sgpr_kernarg_preload_offset 0
		.amdhsa_user_sgpr_private_segment_size 0
		.amdhsa_uses_dynamic_stack 0
		.amdhsa_enable_private_segment 0
		.amdhsa_system_sgpr_workgroup_id_x 1
		.amdhsa_system_sgpr_workgroup_id_y 0
		.amdhsa_system_sgpr_workgroup_id_z 0
		.amdhsa_system_sgpr_workgroup_info 0
		.amdhsa_system_vgpr_workitem_id 0
		.amdhsa_next_free_vgpr 46
		.amdhsa_next_free_sgpr 64
		.amdhsa_accum_offset 48
		.amdhsa_reserve_vcc 1
		.amdhsa_float_round_mode_32 0
		.amdhsa_float_round_mode_16_64 0
		.amdhsa_float_denorm_mode_32 3
		.amdhsa_float_denorm_mode_16_64 3
		.amdhsa_dx10_clamp 1
		.amdhsa_ieee_mode 1
		.amdhsa_fp16_overflow 0
		.amdhsa_tg_split 0
		.amdhsa_exception_fp_ieee_invalid_op 0
		.amdhsa_exception_fp_denorm_src 0
		.amdhsa_exception_fp_ieee_div_zero 0
		.amdhsa_exception_fp_ieee_overflow 0
		.amdhsa_exception_fp_ieee_underflow 0
		.amdhsa_exception_fp_ieee_inexact 0
		.amdhsa_exception_int_div_zero 0
	.end_amdhsa_kernel

amdhsa.kernels:
  - .agpr_count:     0
    .args:
      - .actual_access:  read_only
        .address_space:  global
        .offset:         0
        .size:           8
        .value_kind:     global_buffer
      - .actual_access:  read_only
        .address_space:  global
        .offset:         8
        .size:           8
        .value_kind:     global_buffer
      - .actual_access:  read_only
        .address_space:  global
        .offset:         16
        .size:           8
        .value_kind:     global_buffer
      - .actual_access:  write_only
        .address_space:  global
        .offset:         24
        .size:           8
        .value_kind:     global_buffer
      - .offset:         32
        .size:           4
        .value_kind:     hidden_block_count_x
      - .offset:         36
        .size:           4
        .value_kind:     hidden_block_count_y
      - .offset:         40
        .size:           4
        .value_kind:     hidden_block_count_z
      - .offset:         44
        .size:           2
        .value_kind:     hidden_group_size_x
      - .offset:         46
        .size:           2
        .value_kind:     hidden_group_size_y
      - .offset:         48
        .size:           2
        .value_kind:     hidden_group_size_z
      - .offset:         50
        .size:           2
        .value_kind:     hidden_remainder_x
      - .offset:         52
        .size:           2
        .value_kind:     hidden_remainder_y
      - .offset:         54
        .size:           2
        .value_kind:     hidden_remainder_z
      - .offset:         72
        .size:           8
        .value_kind:     hidden_global_offset_x
      - .offset:         80
        .size:           8
        .value_kind:     hidden_global_offset_y
      - .offset:         88
        .size:           8
        .value_kind:     hidden_global_offset_z
      - .offset:         96
        .size:           2
        .value_kind:     hidden_grid_dims
    .group_segment_fixed_size: 0
    .kernarg_segment_align: 8
    .kernarg_segment_size: 288
    .language:       OpenCL C
    .language_version:
      - 2
      - 0
    .max_flat_workgroup_size: 1024
    .name:           _Z13prep_w_kernelPKfS0_S0_PDv8_DF16_
    .private_segment_fixed_size: 0
    .sgpr_count:     18
    .sgpr_spill_count: 0
    .symbol:         _Z13prep_w_kernelPKfS0_S0_PDv8_DF16_.kd
    .uniform_work_group_size: 1
    .uses_dynamic_stack: false
    .vgpr_count:     15
    .vgpr_spill_count: 0
    .wavefront_size: 64
  - .agpr_count:     0
    .args:
      - .actual_access:  read_only
        .address_space:  global
        .offset:         0
        .size:           8
        .value_kind:     global_buffer
      - .actual_access:  read_only
        .address_space:  global
        .offset:         8
        .size:           8
        .value_kind:     global_buffer
      - .actual_access:  write_only
        .address_space:  global
        .offset:         16
        .size:           8
        .value_kind:     global_buffer
      - .actual_access:  write_only
        .address_space:  global
        .offset:         24
        .size:           8
        .value_kind:     global_buffer
      - .actual_access:  write_only
        .address_space:  global
        .offset:         32
        .size:           8
        .value_kind:     global_buffer
    .group_segment_fixed_size: 131072
    .kernarg_segment_align: 8
    .kernarg_segment_size: 40
    .language:       OpenCL C
    .language_version:
      - 2
      - 0
    .max_flat_workgroup_size: 512
    .name:           _Z11proj_kernelPKfPKDv8_DF16_PDF16_S4_S4_
    .private_segment_fixed_size: 0
    .sgpr_count:     26
    .sgpr_spill_count: 0
    .symbol:         _Z11proj_kernelPKfPKDv8_DF16_PDF16_S4_S4_.kd
    .uniform_work_group_size: 1
    .uses_dynamic_stack: false
    .vgpr_count:     158
    .vgpr_spill_count: 0
    .wavefront_size: 64
  - .agpr_count:     0
    .args:
      - .actual_access:  read_only
        .address_space:  global
        .offset:         0
        .size:           8
        .value_kind:     global_buffer
      - .address_space:  global
        .offset:         8
        .size:           8
        .value_kind:     global_buffer
      - .address_space:  global
        .offset:         16
        .size:           8
        .value_kind:     global_buffer
      - .actual_access:  write_only
        .address_space:  global
        .offset:         24
        .size:           8
        .value_kind:     global_buffer
      - .actual_access:  write_only
        .address_space:  global
        .offset:         32
        .size:           8
        .value_kind:     global_buffer
      - .actual_access:  write_only
        .address_space:  global
        .offset:         40
        .size:           8
        .value_kind:     global_buffer
    .group_segment_fixed_size: 65536
    .kernarg_segment_align: 8
    .kernarg_segment_size: 48
    .language:       OpenCL C
    .language_version:
      - 2
      - 0
    .max_flat_workgroup_size: 512
    .name:           _Z11attn_kernelPKDF16_S0_S0_PfPDF16_S1_
    .private_segment_fixed_size: 0
    .sgpr_count:     73
    .sgpr_spill_count: 0
    .symbol:         _Z11attn_kernelPKDF16_S0_S0_PfPDF16_S1_.kd
    .uniform_work_group_size: 1
    .uses_dynamic_stack: false
    .vgpr_count:     114
    .vgpr_spill_count: 0
    .wavefront_size: 64
  - .agpr_count:     0
    .args:
      - .actual_access:  read_only
        .address_space:  global
        .offset:         0
        .size:           8
        .value_kind:     global_buffer
      - .actual_access:  read_only
        .address_space:  global
        .offset:         8
        .size:           8
        .value_kind:     global_buffer
      - .actual_access:  write_only
        .address_space:  global
        .offset:         16
        .size:           8
        .value_kind:     global_buffer
    .group_segment_fixed_size: 0
    .kernarg_segment_align: 8
    .kernarg_segment_size: 24
    .language:       OpenCL C
    .language_version:
      - 2
      - 0
    .max_flat_workgroup_size: 256
    .name:           _Z14combine_kernelPKDF16_PKfPf
    .private_segment_fixed_size: 0
    .sgpr_count:     70
    .sgpr_spill_count: 0
    .symbol:         _Z14combine_kernelPKDF16_PKfPf.kd
    .uniform_work_group_size: 1
    .uses_dynamic_stack: false
    .vgpr_count:     46
    .vgpr_spill_count: 0
    .wavefront_size: 64
